# gather tails merged into one round trip; census moved to idle wave during layer 1
# baseline (speedup 1.0000x reference)
.LBB2_265:
	s_mulk_i32 s64, 0x190
	v_lshrrev_b32_e32 v2, 1, v0
	s_movk_i32 s2, 0x320
	v_cmp_gt_u32_e32 vcc, s2, v0
	v_add_u32_e32 v64, s64, v2
	s_mov_b32 s2, 0x186a0
	v_cmp_gt_i32_e64 s[2:3], s2, v64
	s_and_b64 s[8:9], vcc, s[2:3]
	v_mov_b32_e32 v46, 0
	v_mov_b32_e32 v47, 0
	s_and_saveexec_b64 s[2:3], s[8:9]
	v_mov_b32_e32 v3, 0x16e00
	v_lshl_add_u32 v2, v2, 2, v3
	ds_read2_b32 v[46:47], v2 offset1:1
	s_or_b64 exec, exec, s[2:3]
	s_waitcnt lgkmcnt(0)
	v_sub_u32_e32 v2, v47, v46
	v_cvt_f32_u32_e32 v2, v2
	v_and_b32_e32 v44, 1, v0
	v_max_f32_e32 v2, 1.0, v2
	v_rsq_f32_e32 v53, v2
	v_readfirstlane_b32 s85, v0
	s_lshr_b32 s85, s85, 6
	s_cmp_lg_u32 s85, 15
	s_cbranch_scc1 .Lcensus_skip
	s_mov_b64 s[86:87], exec
	s_mov_b64 exec, 1
	v_mov_b32_e32 v66, 0
	v_mov_b32_e32 v67, 0x1000
	s_lshl_b32 s88, s33, 8
	s_addk_i32 s88, 0x400
	v_mov_b32_e32 v68, s88
	s_mov_b32 s89, 0
.Lcensus_loop:
	global_load_dword v69, v66, s[54:55] offset:1024 sc1
	global_load_dword v70, v66, s[54:55] offset:1280 sc1
	global_load_dword v71, v66, s[54:55] offset:1536 sc1
	global_load_dword v72, v66, s[54:55] offset:1792 sc1
	global_load_dword v73, v66, s[54:55] offset:2048 sc1
	global_load_dword v74, v66, s[54:55] offset:2304 sc1
	global_load_dword v75, v66, s[54:55] offset:2560 sc1
	global_load_dword v76, v66, s[54:55] offset:2816 sc1
	global_load_dword v77, v66, s[54:55] offset:3072 sc1
	global_load_dword v78, v66, s[54:55] offset:3328 sc1
	global_load_dword v79, v66, s[54:55] offset:3584 sc1
	global_load_dword v80, v66, s[54:55] offset:3840 sc1
	global_load_dword v81, v67, s[54:55] offset:0 sc1
	global_load_dword v82, v67, s[54:55] offset:256 sc1
	global_load_dword v83, v67, s[54:55] offset:512 sc1
	global_load_dword v84, v67, s[54:55] offset:768 sc1
	global_load_dword v85, v68, s[54:55] sc1
	s_waitcnt vmcnt(0)
	v_add_u32_e32 v86, v69, v70
	v_add_u32_e32 v86, v86, v71
	v_add_u32_e32 v86, v86, v72
	v_add_u32_e32 v86, v86, v73
	v_add_u32_e32 v86, v86, v74
	v_add_u32_e32 v86, v86, v75
	v_add_u32_e32 v86, v86, v76
	v_add_u32_e32 v86, v86, v77
	v_add_u32_e32 v86, v86, v78
	v_add_u32_e32 v86, v86, v79
	v_add_u32_e32 v86, v86, v80
	v_add_u32_e32 v86, v86, v81
	v_add_u32_e32 v86, v86, v82
	v_add_u32_e32 v86, v86, v83
	v_add_u32_e32 v86, v86, v84
	s_nop 0
	v_readfirstlane_b32 s90, v86
	s_cmpk_eq_u32 s90, 0xfa
	s_cbranch_scc1 .Lcensus_done
	s_sleep 1
	s_add_i32 s89, s89, 1
	s_cmpk_lt_u32 s89, 0x800
	s_cbranch_scc1 .Lcensus_loop
	s_branch .Lcensus_exit
.Lcensus_done:
	v_min_u32_e32 v87, 1, v69
	v_min_u32_e32 v88, 1, v70
	v_add_u32_e32 v87, v87, v88
	v_min_u32_e32 v88, 1, v71
	v_add_u32_e32 v87, v87, v88
	v_min_u32_e32 v88, 1, v72
	v_add_u32_e32 v87, v87, v88
	v_min_u32_e32 v88, 1, v73
	v_add_u32_e32 v87, v87, v88
	v_min_u32_e32 v88, 1, v74
	v_add_u32_e32 v87, v87, v88
	v_min_u32_e32 v88, 1, v75
	v_add_u32_e32 v87, v87, v88
	v_min_u32_e32 v88, 1, v76
	v_add_u32_e32 v87, v87, v88
	v_min_u32_e32 v88, 1, v77
	v_add_u32_e32 v87, v87, v88
	v_min_u32_e32 v88, 1, v78
	v_add_u32_e32 v87, v87, v88
	v_min_u32_e32 v88, 1, v79
	v_add_u32_e32 v87, v87, v88
	v_min_u32_e32 v88, 1, v80
	v_add_u32_e32 v87, v87, v88
	v_min_u32_e32 v88, 1, v81
	v_add_u32_e32 v87, v87, v88
	v_min_u32_e32 v88, 1, v82
	v_add_u32_e32 v87, v87, v88
	v_min_u32_e32 v88, 1, v83
	v_add_u32_e32 v87, v87, v88
	v_min_u32_e32 v88, 1, v84
	v_add_u32_e32 v87, v87, v88
	v_max_u32_e32 v85, 1, v85
	v_max_u32_e32 v87, 1, v87
	v_mov_b32_e32 v88, 0x17d30
	ds_write2_b32 v88, v85, v87 offset1:1
	s_waitcnt lgkmcnt(0)
.Lcensus_exit:
	s_mov_b64 exec, s[86:87]
.Lcensus_skip:
	s_and_saveexec_b64 s[10:11], s[8:9]
	s_cbranch_execz .LBB2_285
	v_lshlrev_b32_e32 v109, 5, v44
	global_load_dwordx4 v[100:103], v109, s[60:61]
	global_load_dwordx4 v[104:107], v109, s[60:61] offset:16
	v_ashrrev_i32_e32 v65, 31, v64
	v_lshl_add_u64 v[110:111], v[64:65], 2, s[58:59]
	global_load_dword v108, v[110:111], off
	s_and_b64 vcc, exec, s[4:5]
	s_cbranch_vccz .LBB2_282
	v_add_u32_e32 v2, 8, v46
	v_mov_b32_e32 v55, 0x3f80
	v_mov_b32_e32 v54, 1.0
	v_cmp_le_u32_e32 vcc, v2, v47
	v_mov_b32_e32 v5, 0
	v_mov_b32_e32 v4, 0
	v_mov_b32_e32 v3, 0
	v_mov_b32_e32 v2, 0
	v_mov_b32_e32 v9, 0
	v_mov_b32_e32 v8, 0
	v_mov_b32_e32 v7, 0
	v_mov_b32_e32 v6, 0
	v_mov_b32_e32 v57, v46
	s_and_saveexec_b64 s[2:3], vcc
	s_cbranch_execz .LBB2_273
	v_mov_b32_e32 v5, 0
	v_mov_b32_e32 v43, v44
	v_lshlrev_b32_e32 v56, 2, v46
	s_mov_b64 s[12:13], 0
	v_mov_b32_e32 v57, v46
	v_mov_b32_e32 v4, v5
	v_mov_b32_e32 v3, v5
	v_mov_b32_e32 v2, v5
	v_mov_b32_e32 v9, v5
	v_mov_b32_e32 v8, v5
	v_mov_b32_e32 v7, v5
	v_mov_b32_e32 v6, v5

.LBB2_273:
	s_or_b64 exec, exec, s[2:3]
	v_sub_u32_e32 v56, v47, v57
	v_cmp_lt_u32_e32 vcc, 0, v56
	s_and_saveexec_b64 s[12:13], vcc
	s_cbranch_execz .LBB2_281
	v_add_u32_e32 v61, -1, v56
	v_lshlrev_b32_e32 v62, 2, v57
	s_mov_b32 s16, 0x3fffe
	ds_read_b32 v10, v62
	v_min_u32_e32 v11, 1, v61
	v_lshl_add_u32 v11, v11, 2, v62
	ds_read_b32 v11, v11
	v_min_u32_e32 v12, 2, v61
	v_lshl_add_u32 v12, v12, 2, v62
	ds_read_b32 v12, v12
	v_min_u32_e32 v13, 3, v61
	v_lshl_add_u32 v13, v13, 2, v62
	ds_read_b32 v13, v13
	v_min_u32_e32 v58, 4, v61
	v_lshl_add_u32 v58, v58, 2, v62
	ds_read_b32 v58, v58
	v_min_u32_e32 v59, 5, v61
	v_lshl_add_u32 v59, v59, 2, v62
	ds_read_b32 v59, v59
	v_min_u32_e32 v60, 6, v61
	v_lshl_add_u32 v60, v60, 2, v62
	ds_read_b32 v60, v60
	s_waitcnt lgkmcnt(6)
	v_lshlrev_b32_e32 v10, 1, v10
	v_and_or_b32 v10, v10, s16, v44
	v_lshlrev_b32_e32 v10, 4, v10
	global_load_dwordx4 v[14:17], v10, s[56:57]
	s_waitcnt lgkmcnt(5)
	v_lshlrev_b32_e32 v11, 1, v11
	v_and_or_b32 v11, v11, s16, v44
	v_lshlrev_b32_e32 v11, 4, v11
	global_load_dwordx4 v[18:21], v11, s[56:57]
	s_waitcnt lgkmcnt(4)
	v_lshlrev_b32_e32 v12, 1, v12
	v_and_or_b32 v12, v12, s16, v44
	v_lshlrev_b32_e32 v12, 4, v12
	global_load_dwordx4 v[22:25], v12, s[56:57]
	s_waitcnt lgkmcnt(3)
	v_lshlrev_b32_e32 v13, 1, v13
	v_and_or_b32 v13, v13, s16, v44
	v_lshlrev_b32_e32 v13, 4, v13
	global_load_dwordx4 v[26:29], v13, s[56:57]
	s_waitcnt lgkmcnt(2)
	v_lshlrev_b32_e32 v58, 1, v58
	v_and_or_b32 v58, v58, s16, v44
	v_lshlrev_b32_e32 v58, 4, v58
	global_load_dwordx4 v[30:33], v58, s[56:57]
	s_waitcnt lgkmcnt(1)
	v_lshlrev_b32_e32 v59, 1, v59
	v_and_or_b32 v59, v59, s16, v44
	v_lshlrev_b32_e32 v59, 4, v59
	global_load_dwordx4 v[34:37], v59, s[56:57]
	s_waitcnt lgkmcnt(0)
	v_lshlrev_b32_e32 v60, 1, v60
	v_and_or_b32 v60, v60, s16, v44
	v_lshlrev_b32_e32 v60, 4, v60
	global_load_dwordx4 v[38:41], v60, s[56:57]
	s_waitcnt vmcnt(6)
	v_dot2c_f32_bf16_e32 v6, v14, v55
	v_dot2c_f32_bf16_e32 v7, v14, v54
	v_dot2c_f32_bf16_e32 v8, v15, v55
	v_dot2c_f32_bf16_e32 v9, v15, v54
	v_dot2c_f32_bf16_e32 v2, v16, v55
	v_dot2c_f32_bf16_e32 v3, v16, v54
	v_dot2c_f32_bf16_e32 v4, v17, v55
	v_dot2c_f32_bf16_e32 v5, v17, v54
	v_cmp_lt_u32_e32 vcc, 1, v56
	s_and_b64 exec, exec, vcc
	s_waitcnt vmcnt(5)
	v_dot2c_f32_bf16_e32 v6, v18, v55
	v_dot2c_f32_bf16_e32 v7, v18, v54
	v_dot2c_f32_bf16_e32 v8, v19, v55
	v_dot2c_f32_bf16_e32 v9, v19, v54
	v_dot2c_f32_bf16_e32 v2, v20, v55
	v_dot2c_f32_bf16_e32 v3, v20, v54
	v_dot2c_f32_bf16_e32 v4, v21, v55
	v_dot2c_f32_bf16_e32 v5, v21, v54
	v_cmp_lt_u32_e32 vcc, 2, v56
	s_and_b64 exec, exec, vcc
	s_waitcnt vmcnt(4)
	v_dot2c_f32_bf16_e32 v6, v22, v55
	v_dot2c_f32_bf16_e32 v7, v22, v54
	v_dot2c_f32_bf16_e32 v8, v23, v55
	v_dot2c_f32_bf16_e32 v9, v23, v54
	v_dot2c_f32_bf16_e32 v2, v24, v55
	v_dot2c_f32_bf16_e32 v3, v24, v54
	v_dot2c_f32_bf16_e32 v4, v25, v55
	v_dot2c_f32_bf16_e32 v5, v25, v54
	v_cmp_lt_u32_e32 vcc, 3, v56
	s_and_b64 exec, exec, vcc
	s_waitcnt vmcnt(3)
	v_dot2c_f32_bf16_e32 v6, v26, v55
	v_dot2c_f32_bf16_e32 v7, v26, v54
	v_dot2c_f32_bf16_e32 v8, v27, v55
	v_dot2c_f32_bf16_e32 v9, v27, v54
	v_dot2c_f32_bf16_e32 v2, v28, v55
	v_dot2c_f32_bf16_e32 v3, v28, v54
	v_dot2c_f32_bf16_e32 v4, v29, v55
	v_dot2c_f32_bf16_e32 v5, v29, v54
	v_cmp_lt_u32_e32 vcc, 4, v56
	s_and_b64 exec, exec, vcc
	s_waitcnt vmcnt(2)
	v_dot2c_f32_bf16_e32 v6, v30, v55
	v_dot2c_f32_bf16_e32 v7, v30, v54
	v_dot2c_f32_bf16_e32 v8, v31, v55
	v_dot2c_f32_bf16_e32 v9, v31, v54
	v_dot2c_f32_bf16_e32 v2, v32, v55
	v_dot2c_f32_bf16_e32 v3, v32, v54
	v_dot2c_f32_bf16_e32 v4, v33, v55
	v_dot2c_f32_bf16_e32 v5, v33, v54
	v_cmp_lt_u32_e32 vcc, 5, v56
	s_and_b64 exec, exec, vcc
	s_waitcnt vmcnt(1)
	v_dot2c_f32_bf16_e32 v6, v34, v55
	v_dot2c_f32_bf16_e32 v7, v34, v54
	v_dot2c_f32_bf16_e32 v8, v35, v55
	v_dot2c_f32_bf16_e32 v9, v35, v54
	v_dot2c_f32_bf16_e32 v2, v36, v55
	v_dot2c_f32_bf16_e32 v3, v36, v54
	v_dot2c_f32_bf16_e32 v4, v37, v55
	v_dot2c_f32_bf16_e32 v5, v37, v54
	v_cmp_lt_u32_e32 vcc, 6, v56
	s_and_b64 exec, exec, vcc
	s_waitcnt vmcnt(0)
	v_dot2c_f32_bf16_e32 v6, v38, v55
	v_dot2c_f32_bf16_e32 v7, v38, v54
	v_dot2c_f32_bf16_e32 v8, v39, v55
	v_dot2c_f32_bf16_e32 v9, v39, v54
	v_dot2c_f32_bf16_e32 v2, v40, v55
	v_dot2c_f32_bf16_e32 v3, v40, v54
	v_dot2c_f32_bf16_e32 v4, v41, v55
	v_dot2c_f32_bf16_e32 v5, v41, v54

.LBB2_356:
	s_or_b64 exec, exec, s[0:1]
	v_sub_u32_e32 v1, v47, v46
	v_cmp_lt_u32_e32 vcc, 0, v1
	s_and_saveexec_b64 s[2:3], vcc
	s_cbranch_execz .LBB2_364
	v_add_u32_e32 v45, -1, v1
	v_lshlrev_b32_e32 v54, 2, v46
	s_mov_b32 s6, 0x3fffe
	ds_read_b32 v10, v54
	v_min_u32_e32 v11, 1, v45
	v_lshl_add_u32 v11, v11, 2, v54
	ds_read_b32 v11, v11
	v_min_u32_e32 v12, 2, v45
	v_lshl_add_u32 v12, v12, 2, v54
	ds_read_b32 v12, v12
	v_min_u32_e32 v13, 3, v45
	v_lshl_add_u32 v13, v13, 2, v54
	ds_read_b32 v13, v13
	v_min_u32_e32 v48, 4, v45
	v_lshl_add_u32 v48, v48, 2, v54
	ds_read_b32 v48, v48
	v_min_u32_e32 v49, 5, v45
	v_lshl_add_u32 v49, v49, 2, v54
	ds_read_b32 v49, v49
	v_min_u32_e32 v50, 6, v45
	v_lshl_add_u32 v50, v50, 2, v54
	ds_read_b32 v50, v50
	s_waitcnt lgkmcnt(6)
	v_lshlrev_b32_e32 v10, 1, v10
	v_and_or_b32 v10, v10, s6, v44
	v_lshlrev_b32_e32 v10, 4, v10
	global_load_dwordx4 v[14:17], v10, s[62:63]
	s_waitcnt lgkmcnt(5)
	v_lshlrev_b32_e32 v11, 1, v11
	v_and_or_b32 v11, v11, s6, v44
	v_lshlrev_b32_e32 v11, 4, v11
	global_load_dwordx4 v[18:21], v11, s[62:63]
	s_waitcnt lgkmcnt(4)
	v_lshlrev_b32_e32 v12, 1, v12
	v_and_or_b32 v12, v12, s6, v44
	v_lshlrev_b32_e32 v12, 4, v12
	global_load_dwordx4 v[22:25], v12, s[62:63]
	s_waitcnt lgkmcnt(3)
	v_lshlrev_b32_e32 v13, 1, v13
	v_and_or_b32 v13, v13, s6, v44
	v_lshlrev_b32_e32 v13, 4, v13
	global_load_dwordx4 v[26:29], v13, s[62:63]
	s_waitcnt lgkmcnt(2)
	v_lshlrev_b32_e32 v48, 1, v48
	v_and_or_b32 v48, v48, s6, v44
	v_lshlrev_b32_e32 v48, 4, v48
	global_load_dwordx4 v[30:33], v48, s[62:63]
	s_waitcnt lgkmcnt(1)
	v_lshlrev_b32_e32 v49, 1, v49
	v_and_or_b32 v49, v49, s6, v44
	v_lshlrev_b32_e32 v49, 4, v49
	global_load_dwordx4 v[34:37], v49, s[62:63]
	s_waitcnt lgkmcnt(0)
	v_lshlrev_b32_e32 v50, 1, v50
	v_and_or_b32 v50, v50, s6, v44
	v_lshlrev_b32_e32 v50, 4, v50
	global_load_dwordx4 v[38:41], v50, s[62:63]
	s_waitcnt vmcnt(6)
	v_dot2c_f32_bf16_e32 v6, v14, v43
	v_dot2c_f32_bf16_e32 v7, v14, v42
	v_dot2c_f32_bf16_e32 v8, v15, v43
	v_dot2c_f32_bf16_e32 v9, v15, v42
	v_dot2c_f32_bf16_e32 v2, v16, v43
	v_dot2c_f32_bf16_e32 v3, v16, v42
	v_dot2c_f32_bf16_e32 v4, v17, v43
	v_dot2c_f32_bf16_e32 v5, v17, v42
	v_cmp_lt_u32_e32 vcc, 1, v1
	s_and_b64 exec, exec, vcc
	s_waitcnt vmcnt(5)
	v_dot2c_f32_bf16_e32 v6, v18, v43
	v_dot2c_f32_bf16_e32 v7, v18, v42
	v_dot2c_f32_bf16_e32 v8, v19, v43
	v_dot2c_f32_bf16_e32 v9, v19, v42
	v_dot2c_f32_bf16_e32 v2, v20, v43
	v_dot2c_f32_bf16_e32 v3, v20, v42
	v_dot2c_f32_bf16_e32 v4, v21, v43
	v_dot2c_f32_bf16_e32 v5, v21, v42
	v_cmp_lt_u32_e32 vcc, 2, v1
	s_and_b64 exec, exec, vcc
	s_waitcnt vmcnt(4)
	v_dot2c_f32_bf16_e32 v6, v22, v43
	v_dot2c_f32_bf16_e32 v7, v22, v42
	v_dot2c_f32_bf16_e32 v8, v23, v43
	v_dot2c_f32_bf16_e32 v9, v23, v42
	v_dot2c_f32_bf16_e32 v2, v24, v43
	v_dot2c_f32_bf16_e32 v3, v24, v42
	v_dot2c_f32_bf16_e32 v4, v25, v43
	v_dot2c_f32_bf16_e32 v5, v25, v42
	v_cmp_lt_u32_e32 vcc, 3, v1
	s_and_b64 exec, exec, vcc
	s_waitcnt vmcnt(3)
	v_dot2c_f32_bf16_e32 v6, v26, v43
	v_dot2c_f32_bf16_e32 v7, v26, v42
	v_dot2c_f32_bf16_e32 v8, v27, v43
	v_dot2c_f32_bf16_e32 v9, v27, v42
	v_dot2c_f32_bf16_e32 v2, v28, v43
	v_dot2c_f32_bf16_e32 v3, v28, v42
	v_dot2c_f32_bf16_e32 v4, v29, v43
	v_dot2c_f32_bf16_e32 v5, v29, v42
	v_cmp_lt_u32_e32 vcc, 4, v1
	s_and_b64 exec, exec, vcc
	s_waitcnt vmcnt(2)
	v_dot2c_f32_bf16_e32 v6, v30, v43
	v_dot2c_f32_bf16_e32 v7, v30, v42
	v_dot2c_f32_bf16_e32 v8, v31, v43
	v_dot2c_f32_bf16_e32 v9, v31, v42
	v_dot2c_f32_bf16_e32 v2, v32, v43
	v_dot2c_f32_bf16_e32 v3, v32, v42
	v_dot2c_f32_bf16_e32 v4, v33, v43
	v_dot2c_f32_bf16_e32 v5, v33, v42
	v_cmp_lt_u32_e32 vcc, 5, v1
	s_and_b64 exec, exec, vcc
	s_waitcnt vmcnt(1)
	v_dot2c_f32_bf16_e32 v6, v34, v43
	v_dot2c_f32_bf16_e32 v7, v34, v42
	v_dot2c_f32_bf16_e32 v8, v35, v43
	v_dot2c_f32_bf16_e32 v9, v35, v42
	v_dot2c_f32_bf16_e32 v2, v36, v43
	v_dot2c_f32_bf16_e32 v3, v36, v42
	v_dot2c_f32_bf16_e32 v4, v37, v43
	v_dot2c_f32_bf16_e32 v5, v37, v42
	v_cmp_lt_u32_e32 vcc, 6, v1
	s_and_b64 exec, exec, vcc
	s_waitcnt vmcnt(0)
	v_dot2c_f32_bf16_e32 v6, v38, v43
	v_dot2c_f32_bf16_e32 v7, v38, v42
	v_dot2c_f32_bf16_e32 v8, v39, v43
	v_dot2c_f32_bf16_e32 v9, v39, v42
	v_dot2c_f32_bf16_e32 v2, v40, v43
	v_dot2c_f32_bf16_e32 v3, v40, v42
	v_dot2c_f32_bf16_e32 v4, v41, v43
	v_dot2c_f32_bf16_e32 v5, v41, v42
